# lru_a: per-task gate-weight copy loop unrolled (4 loads in flight, one wait) on top of router/nops/logf/hg_a/attention edits
# speedup vs baseline: 1.0051x; 1.0012x over previous
; #define LAS __attribute__((address_space(3)))
; __device__ __forceinline__ void ph_lru_a(const Frame& F, int jj) {
;     ...
;     for (int task = F.wg; task < NTASK; task += F.G) {
;         const int grp = task % 11, kb = (task / 11) & 15, b = task / (11 * 16);
;         __syncthreads();
;         for (int i = F.tid; i < 4 * 4096 / 8; i += 512) { const int mg = i >> 9, r = i & 511;
;             *(LAS u32x4*)(Wl + (mg * 64 + (r >> 3)) * 72 + (r & 7) * 8) = *(const u32x4*)(wsrc + ((size_t)mg * 16 + kb) * 4096 + r * 8); }
.LBB0_439:
	s_mul_hi_i32 s13, s11, 0x2e8ba2e9
	s_lshr_b32 s16, s13, 31
	s_ashr_i32 s10, s13, 1
	s_add_i32 s10, s10, s16
	s_and_b32 s2, s10, 15
	s_waitcnt vmcnt(0)
	s_barrier
	s_and_saveexec_b64 s[6:7], s[42:43]
	s_movk_i32 s14, 0x90
	s_cbranch_execz .LBB0_442
	s_lshl_b32 s64, s2, 13
	v_lshl_add_u64 v[4:5], v[92:93], 0, s[64:65]
	s_mov_b64 s[8:9], 0x20000
	global_load_dwordx4 v[210:213], v[4:5], off
	v_lshl_add_u64 v[226:227], v[4:5], 0, s[8:9]
	global_load_dwordx4 v[214:217], v[226:227], off
	v_lshl_add_u64 v[226:227], v[226:227], 0, s[8:9]
	global_load_dwordx4 v[218:221], v[226:227], off
	v_lshl_add_u64 v[226:227], v[226:227], 0, s[8:9]
	global_load_dwordx4 v[222:225], v[226:227], off
	v_and_b32_e32 v13, 56, v118
	s_movk_i32 s17, 0x5ff
	v_lshlrev_b32_e32 v13, 1, v13
	v_mul_lo_u32 v12, v105, s14
	v_add3_u32 v12, 0, v12, v13
	s_waitcnt vmcnt(0)
	ds_write_b128 v12, v[210:213]
	ds_write_b128 v12, v[214:217] offset:9216
	ds_write_b128 v12, v[218:221] offset:18432
	ds_write_b128 v12, v[222:225] offset:27648
